# loop-edge rotation (strategy 9) in the attention main loop (loop-carried updates moved in front of the closing tile barrier) + P4 skinny meta-row residual loads issued together; on top of v51
# speedup vs baseline: 1.0179x; 1.0018x over previous
.LBB0_1702:
	s_mov_b32 s8, s53
	s_mov_b32 s41, s52
	ds_read_b128 v[36:39], v35
	ds_read_b128 v[40:43], v35 offset:32
	ds_read_b128 v[44:47], v35 offset:64
	ds_read_b128 v[82:85], v35 offset:96
	ds_read_b128 v[178:181], v35 offset:128
	ds_read_b128 v[86:89], v35 offset:160
	ds_read_b128 v[90:93], v35 offset:192
	ds_read_b128 v[94:97], v35 offset:224
	s_waitcnt lgkmcnt(4)
	v_sub_f32_e32 v113, v213, v85
	v_sub_f32_e32 v112, v213, v84
	v_sub_f32_e32 v111, v213, v83
	v_sub_f32_e32 v110, v213, v82
	v_sub_f32_e32 v109, v213, v47
	v_sub_f32_e32 v108, v213, v46
	v_sub_f32_e32 v107, v213, v45
	v_sub_f32_e32 v106, v213, v44
	v_sub_f32_e32 v105, v213, v43
	v_sub_f32_e32 v104, v213, v42
	v_sub_f32_e32 v103, v213, v41
	v_sub_f32_e32 v102, v213, v40
	v_sub_f32_e32 v101, v213, v39
	v_sub_f32_e32 v100, v213, v38
	v_sub_f32_e32 v99, v213, v37
	v_sub_f32_e32 v98, v213, v36
	s_waitcnt lgkmcnt(0)
	v_sub_f32_e32 v97, v213, v97
	v_sub_f32_e32 v96, v213, v96
	v_sub_f32_e32 v95, v213, v95
	v_sub_f32_e32 v94, v213, v94
	v_sub_f32_e32 v93, v213, v93
	v_sub_f32_e32 v92, v213, v92
	v_sub_f32_e32 v91, v213, v91
	v_sub_f32_e32 v90, v213, v90
	v_sub_f32_e32 v89, v213, v89
	v_sub_f32_e32 v88, v213, v88
	v_sub_f32_e32 v87, v213, v87
	v_sub_f32_e32 v86, v213, v86
	v_sub_f32_e32 v85, v213, v181
	v_sub_f32_e32 v84, v213, v180
	v_sub_f32_e32 v83, v213, v179
	v_sub_f32_e32 v82, v213, v178
	v_add_u32_e32 v178, s42, v235
	ds_read_b64_tr_b16 v[36:37], v178 offset:24576
	ds_read_b64_tr_b16 v[38:39], v178 offset:25088
	v_add_f32_e32 v40, v66, v67
	v_add_f32_e32 v40, v68, v40
	v_add_f32_e32 v40, v69, v40
	v_add_f32_e32 v40, v70, v40
	v_add_f32_e32 v44, v71, v40
	v_cvt_pk_bf16_f32 v130, v66, v67
	v_cvt_pk_bf16_f32 v131, v68, v69
	v_mfma_f32_32x32x16_bf16 v[98:113], v[174:177], v[114:117], v[98:113]
	ds_read_b64_tr_b16 v[40:41], v178 offset:28672
	ds_read_b64_tr_b16 v[42:43], v178 offset:29184
	v_add_f32_e32 v44, v72, v44
	v_add_f32_e32 v44, v73, v44
	v_add_f32_e32 v44, v74, v44
	v_add_f32_e32 v48, v75, v44
	v_cvt_pk_bf16_f32 v132, v70, v71
	v_cvt_pk_bf16_f32 v133, v72, v73
	v_mfma_f32_32x32x16_bf16 v[82:97], v[166:169], v[114:117], v[82:97]
	ds_read_b64_tr_b16 v[44:45], v178 offset:25600
	ds_read_b64_tr_b16 v[46:47], v178 offset:26112
	v_add_f32_e32 v48, v76, v48
	v_add_f32_e32 v48, v77, v48
	v_add_f32_e32 v48, v78, v48
	v_add_f32_e32 v48, v79, v48
	v_cvt_pk_bf16_f32 v134, v74, v75
	v_cvt_pk_bf16_f32 v135, v76, v77
	v_mfma_f32_32x32x16_bf16 v[98:113], v[170:173], v[118:121], v[98:113]
	ds_read_b64_tr_b16 v[66:67], v178 offset:29696
	ds_read_b64_tr_b16 v[68:69], v178 offset:30208
	v_add_f32_e32 v48, v80, v48
	v_add_f32_e32 v48, v81, v48
	v_add_f32_e32 v48, v50, v48
	v_add_f32_e32 v48, v51, v48
	v_cvt_pk_bf16_f32 v136, v78, v79
	v_cvt_pk_bf16_f32 v137, v80, v81
	v_mfma_f32_32x32x16_bf16 v[82:97], v[158:161], v[118:121], v[82:97]
	ds_read_b64_tr_b16 v[158:159], v178 offset:26624
	ds_read_b64_tr_b16 v[160:161], v178 offset:27136
	v_add_f32_e32 v48, v52, v48
	v_add_f32_e32 v48, v53, v48
	v_add_f32_e32 v48, v54, v48
	v_add_f32_e32 v70, v55, v48
	v_cvt_pk_bf16_f32 v138, v50, v51
	v_cvt_pk_bf16_f32 v139, v52, v53
	v_mfma_f32_32x32x16_bf16 v[98:113], v[162:165], v[122:125], v[98:113]
	ds_read_b64_tr_b16 v[48:49], v178 offset:30720
	ds_read_b64_tr_b16 v[50:51], v178 offset:31232
	v_add_f32_e32 v52, v56, v70
	v_add_f32_e32 v52, v57, v52
	v_add_f32_e32 v52, v58, v52
	v_add_f32_e32 v52, v59, v52
	v_cvt_pk_bf16_f32 v140, v54, v55
	v_cvt_pk_bf16_f32 v141, v56, v57
	v_mfma_f32_32x32x16_bf16 v[82:97], v[150:153], v[122:125], v[82:97]
	ds_read_b64_tr_b16 v[150:151], v178 offset:27648
	ds_read_b64_tr_b16 v[152:153], v178 offset:28160
	v_add_f32_e32 v52, v60, v52
	v_add_f32_e32 v52, v61, v52
	v_add_f32_e32 v52, v62, v52
	v_add_f32_e32 v52, v63, v52
	v_cvt_pk_bf16_f32 v142, v58, v59
	v_cvt_pk_bf16_f32 v143, v60, v61
	v_mfma_f32_32x32x16_bf16 v[98:113], v[154:157], v[126:129], v[98:113]
	ds_read_b64_tr_b16 v[166:167], v178 offset:31744
	ds_read_b64_tr_b16 v[168:169], v178 offset:32256
	v_add_f32_e32 v52, v64, v52
	v_add_f32_e32 v52, v65, v52
	v_add_f32_e32 v251, 0, v52
	v_cvt_pk_bf16_f32 v144, v62, v63
	v_cvt_pk_bf16_f32 v145, v64, v65
	v_mfma_f32_32x32x16_bf16 v[82:97], v[146:149], v[126:129], v[82:97]
	v_lshl_add_u64 v[52:53], v[220:221], 0, s[20:21]
	s_add_i32 s42, s52, s50
	s_mov_b32 s43, m0
	s_mov_b32 m0, s42
	s_nop 0
	global_load_lds_dwordx4 v[52:53], off
	s_mov_b32 m0, s43
	v_lshl_add_u64 v[52:53], v[218:219], 0, s[20:21]
	s_add_i32 s42, s53, s51
	s_mov_b32 s43, m0
	s_mov_b32 m0, s42
	s_nop 0
	global_load_lds_dwordx4 v[52:53], off
	s_mov_b32 m0, s43
	v_exp_f32_e32 v98, v98
	v_exp_f32_e32 v99, v99
	v_exp_f32_e32 v100, v100
	v_exp_f32_e32 v101, v101
	s_nop 0
	v_exp_f32_e32 v102, v102
	v_exp_f32_e32 v103, v103
	v_exp_f32_e32 v104, v104
	v_exp_f32_e32 v105, v105
	v_add_u32_e32 v52, s8, v232
	ds_read_b128 v[186:189], v52
	ds_read_b128 v[178:181], v52 offset:512
	v_exp_f32_e32 v106, v106
	v_exp_f32_e32 v107, v107
	v_exp_f32_e32 v108, v108
	v_exp_f32_e32 v109, v109
	ds_read_b128 v[182:185], v52 offset:2048
	ds_read_b128 v[170:173], v52 offset:2560
	v_exp_f32_e32 v110, v110
	v_exp_f32_e32 v111, v111
	v_exp_f32_e32 v112, v112
	v_exp_f32_e32 v113, v113
	ds_read_b128 v[174:177], v52 offset:4096
	ds_read_b128 v[154:157], v52 offset:4608
	v_exp_f32_e32 v82, v82
	v_exp_f32_e32 v83, v83
	v_exp_f32_e32 v84, v84
	v_exp_f32_e32 v85, v85
	ds_read_b128 v[162:165], v52 offset:6144
	ds_read_b128 v[146:149], v52 offset:6656
	v_exp_f32_e32 v86, v86
	v_exp_f32_e32 v87, v87
	v_exp_f32_e32 v88, v88
	v_exp_f32_e32 v89, v89
	s_nop 0
	v_exp_f32_e32 v90, v90
	v_exp_f32_e32 v91, v91
	v_exp_f32_e32 v92, v92
	v_exp_f32_e32 v93, v93
	s_nop 0
	v_exp_f32_e32 v94, v94
	v_exp_f32_e32 v95, v95
	v_exp_f32_e32 v96, v96
	v_exp_f32_e32 v97, v97
	s_waitcnt vmcnt(2) lgkmcnt(0)
	s_barrier
	s_add_i32 s42, s53, 0x2000
	s_waitcnt lgkmcnt(14)
	v_mfma_f32_32x32x16_bf16 v[2:17], v[130:133], v[36:39], v[2:17]
	s_cmpk_lg_i32 s53, 0x4000
	v_add_f32_e32 v34, v34, v251
	s_cselect_b32 s52, s42, 0
	v_mfma_f32_32x32x16_bf16 v[18:33], v[130:133], v[40:43], v[18:33]
	ds_read_b128 v[36:39], v35 offset:256
	ds_read_b128 v[40:43], v35 offset:288
	ds_read_b128 v[52:55], v35 offset:320
	ds_read_b128 v[56:59], v35 offset:352
	ds_read_b128 v[242:245], v35 offset:384
	ds_read_b128 v[246:249], v35 offset:416
	ds_read_b128 v[190:193], v35 offset:448
	ds_read_b128 v[60:63], v35 offset:480
	s_waitcnt lgkmcnt(4)
	v_sub_f32_e32 v81, v213, v59
	v_sub_f32_e32 v80, v213, v58
	v_sub_f32_e32 v79, v213, v57
	v_sub_f32_e32 v78, v213, v56
	v_sub_f32_e32 v77, v213, v55
	v_sub_f32_e32 v76, v213, v54
	v_mfma_f32_32x32x16_bf16 v[2:17], v[134:137], v[44:47], v[2:17]
	v_sub_f32_e32 v75, v213, v53
	v_sub_f32_e32 v74, v213, v52
	v_sub_f32_e32 v73, v213, v43
	v_sub_f32_e32 v72, v213, v42
	v_sub_f32_e32 v71, v213, v41
	v_sub_f32_e32 v70, v213, v40
	s_waitcnt lgkmcnt(0)
	v_sub_f32_e32 v65, v213, v63
	v_mfma_f32_32x32x16_bf16 v[18:33], v[134:137], v[66:69], v[18:33]
	v_sub_f32_e32 v69, v213, v39
	v_sub_f32_e32 v68, v213, v38
	v_sub_f32_e32 v67, v213, v37
	v_sub_f32_e32 v66, v213, v36
	v_sub_f32_e32 v64, v213, v62
	v_sub_f32_e32 v63, v213, v61
	v_sub_f32_e32 v62, v213, v60
	v_mfma_f32_32x32x16_bf16 v[2:17], v[138:141], v[158:161], v[2:17]
	v_sub_f32_e32 v61, v213, v193
	v_sub_f32_e32 v60, v213, v192
	v_sub_f32_e32 v59, v213, v191
	v_sub_f32_e32 v58, v213, v190
	v_sub_f32_e32 v57, v213, v249
	v_sub_f32_e32 v56, v213, v248
	v_sub_f32_e32 v55, v213, v247
	v_mfma_f32_32x32x16_bf16 v[18:33], v[138:141], v[48:51], v[18:33]
	v_sub_f32_e32 v54, v213, v246
	v_sub_f32_e32 v53, v213, v245
	v_sub_f32_e32 v52, v213, v244
	v_sub_f32_e32 v51, v213, v243
	v_sub_f32_e32 v50, v213, v242
	v_mfma_f32_32x32x16_bf16 v[2:17], v[142:145], v[150:153], v[2:17]
	v_mfma_f32_32x32x16_bf16 v[18:33], v[142:145], v[166:169], v[18:33]
	v_add_u32_e32 v48, s41, v235
	ds_read_b64_tr_b16 v[36:37], v48 offset:24576
	ds_read_b64_tr_b16 v[38:39], v48 offset:25088
	v_mfma_f32_32x32x16_bf16 v[66:81], v[186:189], v[114:117], v[66:81]
	v_add_f32_e32 v40, v98, v99
	v_add_f32_e32 v40, v100, v40
	v_add_f32_e32 v40, v101, v40
	v_add_f32_e32 v40, v102, v40
	v_add_f32_e32 v44, v103, v40
	v_cvt_pk_bf16_f32 v130, v98, v99
	v_cvt_pk_bf16_f32 v131, v100, v101
	ds_read_b64_tr_b16 v[40:41], v48 offset:28672
	ds_read_b64_tr_b16 v[42:43], v48 offset:29184
	v_mfma_f32_32x32x16_bf16 v[50:65], v[178:181], v[114:117], v[50:65]
	v_add_f32_e32 v44, v104, v44
	v_add_f32_e32 v44, v105, v44
	v_add_f32_e32 v44, v106, v44
	v_add_f32_e32 v49, v107, v44
	v_cvt_pk_bf16_f32 v132, v102, v103
	v_cvt_pk_bf16_f32 v133, v104, v105
	ds_read_b64_tr_b16 v[44:45], v48 offset:25600
	ds_read_b64_tr_b16 v[46:47], v48 offset:26112
	v_mfma_f32_32x32x16_bf16 v[66:81], v[182:185], v[118:121], v[66:81]
	v_add_f32_e32 v49, v108, v49
	v_add_f32_e32 v49, v109, v49
	v_add_f32_e32 v49, v110, v49
	v_add_f32_e32 v49, v111, v49
	v_cvt_pk_bf16_f32 v134, v106, v107
	v_cvt_pk_bf16_f32 v135, v108, v109
	ds_read_b64_tr_b16 v[98:99], v48 offset:29696
	ds_read_b64_tr_b16 v[100:101], v48 offset:30208
	v_mfma_f32_32x32x16_bf16 v[50:65], v[170:173], v[118:121], v[50:65]
	v_add_f32_e32 v49, v112, v49
	v_add_f32_e32 v49, v113, v49
	v_add_f32_e32 v49, v82, v49
	v_add_f32_e32 v49, v83, v49
	v_cvt_pk_bf16_f32 v136, v110, v111
	v_cvt_pk_bf16_f32 v137, v112, v113
	ds_read_b64_tr_b16 v[102:103], v48 offset:26624
	ds_read_b64_tr_b16 v[104:105], v48 offset:27136
	v_mfma_f32_32x32x16_bf16 v[66:81], v[174:177], v[122:125], v[66:81]
	v_add_f32_e32 v49, v84, v49
	v_add_f32_e32 v49, v85, v49
	v_add_f32_e32 v49, v86, v49
	v_add_f32_e32 v49, v87, v49
	v_cvt_pk_bf16_f32 v138, v82, v83
	v_cvt_pk_bf16_f32 v139, v84, v85
	ds_read_b64_tr_b16 v[82:83], v48 offset:30720
	ds_read_b64_tr_b16 v[84:85], v48 offset:31232
	v_mfma_f32_32x32x16_bf16 v[50:65], v[154:157], v[122:125], v[50:65]
	v_add_f32_e32 v49, v88, v49
	v_add_f32_e32 v49, v89, v49
	v_add_f32_e32 v49, v90, v49
	v_add_f32_e32 v49, v91, v49
	v_cvt_pk_bf16_f32 v140, v86, v87
	v_cvt_pk_bf16_f32 v141, v88, v89
	ds_read_b64_tr_b16 v[86:87], v48 offset:27648
	ds_read_b64_tr_b16 v[88:89], v48 offset:28160
	v_mfma_f32_32x32x16_bf16 v[66:81], v[162:165], v[126:129], v[66:81]
	v_add_f32_e32 v49, v92, v49
	v_add_f32_e32 v49, v93, v49
	v_add_f32_e32 v49, v94, v49
	v_add_f32_e32 v49, v95, v49
	v_cvt_pk_bf16_f32 v142, v90, v91
	v_cvt_pk_bf16_f32 v143, v92, v93
	ds_read_b64_tr_b16 v[90:91], v48 offset:31744
	ds_read_b64_tr_b16 v[92:93], v48 offset:32256
	v_mfma_f32_32x32x16_bf16 v[50:65], v[146:149], v[126:129], v[50:65]
	v_add_f32_e32 v48, v96, v49
	v_add_f32_e32 v48, v97, v48
	v_add_f32_e32 v48, 0, v48
	v_cvt_pk_bf16_f32 v144, v94, v95
	v_cvt_pk_bf16_f32 v145, v96, v97
	s_add_i32 s41, s53, s50
	s_mov_b32 s42, m0
	s_mov_b32 m0, s41
	s_nop 0
	global_load_lds_dwordx4 v[220:221], off
	s_mov_b32 m0, s42
	s_add_i32 s41, s52, s51
	s_mov_b32 s42, m0
	s_mov_b32 m0, s41
	s_nop 0
	global_load_lds_dwordx4 v[218:219], off
	s_mov_b32 m0, s42
	v_add_f32_e32 v34, v34, v48
	s_add_i32 s30, s30, 2
	s_waitcnt lgkmcnt(14)
	v_mfma_f32_32x32x16_bf16 v[2:17], v[130:133], v[36:39], v[2:17]
	v_exp_f32_e32 v66, v66
	v_exp_f32_e32 v67, v67
	v_exp_f32_e32 v68, v68
	v_exp_f32_e32 v69, v69
	s_waitcnt lgkmcnt(12)
	v_mfma_f32_32x32x16_bf16 v[18:33], v[130:133], v[40:43], v[18:33]
	v_exp_f32_e32 v70, v70
	v_exp_f32_e32 v71, v71
	v_exp_f32_e32 v72, v72
	v_exp_f32_e32 v73, v73
	v_add_u32_e32 v36, s52, v232
	ds_read_b128 v[174:177], v36
	ds_read_b128 v[166:169], v36 offset:512
	s_waitcnt lgkmcnt(12)
	v_mfma_f32_32x32x16_bf16 v[2:17], v[134:137], v[44:47], v[2:17]
	v_exp_f32_e32 v74, v74
	v_exp_f32_e32 v75, v75
	v_exp_f32_e32 v76, v76
	v_exp_f32_e32 v77, v77
	ds_read_b128 v[170:173], v36 offset:2048
	ds_read_b128 v[158:161], v36 offset:2560
	s_waitcnt lgkmcnt(12)
	v_mfma_f32_32x32x16_bf16 v[18:33], v[134:137], v[98:101], v[18:33]
	v_exp_f32_e32 v78, v78
	v_exp_f32_e32 v79, v79
	v_exp_f32_e32 v80, v80
	v_exp_f32_e32 v81, v81
	ds_read_b128 v[162:165], v36 offset:4096
	ds_read_b128 v[150:153], v36 offset:4608
	s_waitcnt lgkmcnt(12)
	v_mfma_f32_32x32x16_bf16 v[2:17], v[138:141], v[102:105], v[2:17]
	v_exp_f32_e32 v50, v50
	v_exp_f32_e32 v51, v51
	v_exp_f32_e32 v52, v52
	v_exp_f32_e32 v53, v53
	ds_read_b128 v[154:157], v36 offset:6144
	ds_read_b128 v[146:149], v36 offset:6656
	s_waitcnt lgkmcnt(12)
	v_mfma_f32_32x32x16_bf16 v[18:33], v[138:141], v[82:85], v[18:33]
	v_exp_f32_e32 v54, v54
	v_exp_f32_e32 v55, v55
	v_exp_f32_e32 v56, v56
	v_exp_f32_e32 v57, v57
	s_waitcnt lgkmcnt(10)
	v_mfma_f32_32x32x16_bf16 v[2:17], v[142:145], v[86:89], v[2:17]
	v_exp_f32_e32 v58, v58
	v_exp_f32_e32 v59, v59
	v_exp_f32_e32 v60, v60
	v_exp_f32_e32 v61, v61
	s_waitcnt lgkmcnt(8)
	v_mfma_f32_32x32x16_bf16 v[18:33], v[142:145], v[90:93], v[18:33]
	v_exp_f32_e32 v62, v62
	v_exp_f32_e32 v63, v63
	v_exp_f32_e32 v64, v64
	v_exp_f32_e32 v65, v65
	s_add_i32 s41, s52, 0x2000
	s_cmpk_lg_i32 s52, 0x4000
	s_cselect_b32 s53, s41, 0
	v_lshl_add_u64 v[218:219], v[218:219], 0, s[14:15]
	v_lshl_add_u64 v[220:221], v[220:221], 0, s[14:15]
	v_add_u32_e32 v35, 0x200, v35
	s_cmp_ge_i32 s30, s9
	s_mov_b32 s42, s8
	s_waitcnt vmcnt(2) lgkmcnt(0)
	s_barrier
	s_cbranch_scc0 .LBB0_1702
	s_add_i32 s9, s30, 1
	s_cmp_ge_i32 s9, s49
	s_cbranch_scc1 .LBB0_1742
